# nt hint on the pooling loads of PROJ's u part (P2 tail, last use)
# baseline (speedup 1.0000x reference)
.LBB0_299:
	s_nop 0
	v_lshl_add_u64 v[4:5], v[18:19], 0, v[14:15]
	v_add_co_u32_e64 v48, s[20:21], s1, v4
	v_add_u32_e32 v7, s37, v105
	s_nop 0
	v_addc_co_u32_e64 v49, s[20:21], 0, v5, s[20:21]
	v_add_u32_e32 v8, s37, v103
	v_add_co_u32_e64 v46, s[20:21], s2, v4
	v_lshl_add_u64 v[2:3], v[20:21], 0, v[14:15]
	v_mov_b32_e32 v6, s37
	s_add_i32 s6, s37, 1
	s_add_i32 s8, s37, 2
	v_add_u32_e32 v9, 1, v7
	v_cmp_lt_i32_e64 s[4:5], s37, v104
	v_add_u32_e32 v51, 1, v8
	v_addc_co_u32_e64 v47, s[20:21], 0, v5, s[20:21]
	v_add_co_u32_e32 v10, vcc, 0x15c00000, v2
	v_add_u32_e32 v12, 2, v7
	v_mov_b32_e32 v13, s6
	v_cmp_lt_i32_e64 s[6:7], s6, v104
	v_add_u32_e32 v23, 3, v7
	v_mov_b32_e32 v25, s8
	v_cmp_lt_i32_e64 s[8:9], s8, v104
	v_add_u32_e32 v52, 2, v8
	v_add_co_u32_e64 v40, s[20:21], s3, v4
	v_cndmask_b32_e64 v6, v9, v6, s[4:5]
	v_cmp_lt_i32_e64 s[4:5], v51, v102
	v_add_u32_e32 v53, 3, v8
	v_add_u32_e32 v54, 4, v8
	v_add_u32_e32 v55, 5, v8
	v_addc_co_u32_e64 v41, s[20:21], 0, v5, s[20:21]
	v_add_u32_e32 v56, 6, v8
	v_add_u32_e32 v57, 7, v8
	v_add_u32_e32 v59, 8, v8
	v_addc_co_u32_e32 v11, vcc, 0, v3, vcc
	v_cndmask_b32_e64 v8, v12, v13, s[6:7]
	v_cndmask_b32_e64 v12, v23, v25, s[8:9]
	v_cndmask_b32_e64 v23, 1.0, 0, s[4:5]
	v_cmp_lt_i32_e64 s[4:5], v52, v102
	v_add_co_u32_e64 v38, s[20:21], s33, v4
	v_add_co_u32_e32 v4, vcc, 0x15c01000, v2
	v_cndmask_b32_e64 v195, 1.0, 0, s[4:5]
	v_cmp_lt_i32_e64 s[4:5], v53, v102
	s_add_i32 s18, s37, 7
	v_addc_co_u32_e64 v39, s[20:21], 0, v5, s[20:21]
	v_cndmask_b32_e64 v197, 1.0, 0, s[4:5]
	v_cmp_lt_i32_e64 s[4:5], v54, v102
	v_addc_co_u32_e32 v5, vcc, 0, v3, vcc
	v_add_u32_e32 v27, 4, v7
	v_add_u32_e32 v31, 5, v7
	v_add_u32_e32 v35, 6, v7
	v_add_u32_e32 v42, 7, v7
	v_add_u32_e32 v7, 8, v7
	v_mov_b32_e32 v50, s18
	v_cmp_lt_i32_e64 s[18:19], s18, v104
	v_cndmask_b32_e64 v199, 1.0, 0, s[4:5]
	v_cmp_lt_i32_e64 s[4:5], v55, v102
	v_add_co_u32_e32 v68, vcc, 0x15c02000, v2
	s_add_i32 s10, s37, 3
	s_add_i32 s12, s37, 4
	s_add_i32 s14, s37, 5
	s_add_i32 s16, s37, 6
	v_cndmask_b32_e64 v66, v7, v50, s[18:19]
	v_min_i32_e32 v25, v51, v102
	v_min_i32_e32 v50, v52, v102
	v_min_i32_e32 v51, v53, v102
	v_min_i32_e32 v52, v54, v102
	v_min_i32_e32 v53, v55, v102
	v_cndmask_b32_e64 v107, 1.0, 0, s[4:5]
	v_min_i32_e32 v54, v56, v102
	v_cmp_lt_i32_e64 s[4:5], v56, v102
	v_min_i32_e32 v55, v57, v102
	v_min_i32_e32 v56, v59, v102
	v_addc_co_u32_e32 v69, vcc, 0, v3, vcc
	v_mov_b32_e32 v29, s10
	v_cmp_lt_i32_e64 s[10:11], s10, v104
	v_mov_b32_e32 v33, s12
	v_cmp_lt_i32_e64 s[12:13], s12, v104
	v_mov_b32_e32 v37, s14
	v_cmp_lt_i32_e64 s[14:15], s14, v104
	v_mov_b32_e32 v44, s16
	v_cmp_lt_i32_e64 s[16:17], s16, v104
	v_cndmask_b32_e64 v106, 1.0, 0, s[4:5]
	v_cmp_lt_i32_e64 s[4:5], v57, v102
	v_cvt_f32_i32_e32 v97, v50
	v_cvt_f32_i32_e32 v98, v51
	v_cvt_f32_i32_e32 v99, v52
	v_cvt_f32_i32_e32 v100, v53
	v_cvt_f32_i32_e32 v101, v54
	v_cvt_f32_i32_e32 v124, v55
	v_cvt_f32_i32_e32 v125, v56
	global_load_dwordx4 v[50:53], v[10:11], off offset:3072 nt
	global_load_dwordx4 v[54:57], v[4:5], off offset:3072 nt
	v_add_co_u32_e32 v4, vcc, 0x15c03000, v2
	v_cndmask_b32_e64 v58, v27, v29, s[10:11]
	v_cndmask_b32_e64 v60, v31, v33, s[12:13]
	v_cndmask_b32_e64 v62, v35, v37, s[14:15]
	v_cndmask_b32_e64 v64, v42, v44, s[16:17]
	v_addc_co_u32_e32 v5, vcc, 0, v3, vcc
	v_cndmask_b32_e64 v44, 1.0, 0, s[4:5]
	v_cmp_lt_i32_e64 s[4:5], v59, v102
	v_ashrrev_i32_e32 v7, 31, v6
	v_ashrrev_i32_e32 v13, 31, v12
	v_ashrrev_i32_e32 v59, 31, v58
	v_ashrrev_i32_e32 v61, 31, v60
	v_ashrrev_i32_e32 v63, 31, v62
	v_ashrrev_i32_e32 v65, 31, v64
	v_ashrrev_i32_e32 v67, 31, v66
	v_add_co_u32_e32 v86, vcc, 0x15c04000, v2
	v_ashrrev_i32_e32 v9, 31, v8
	v_lshlrev_b64 v[6:7], 12, v[6:7]
	v_lshlrev_b64 v[10:11], 12, v[12:13]
	v_lshlrev_b64 v[12:13], 12, v[58:59]
	v_lshlrev_b64 v[58:59], 12, v[60:61]
	v_lshlrev_b64 v[60:61], 12, v[62:63]
	v_lshlrev_b64 v[62:63], 12, v[64:65]
	v_lshlrev_b64 v[64:65], 12, v[66:67]
	v_addc_co_u32_e32 v87, vcc, 0, v3, vcc
	v_lshlrev_b64 v[8:9], 12, v[8:9]
	v_lshl_add_u64 v[6:7], v[16:17], 0, v[6:7]
	v_lshl_add_u64 v[88:89], v[16:17], 0, v[58:59]
	v_lshl_add_u64 v[90:91], v[16:17], 0, v[60:61]
	v_lshl_add_u64 v[92:93], v[16:17], 0, v[62:63]
	v_lshl_add_u64 v[94:95], v[16:17], 0, v[64:65]
	global_load_dwordx4 v[58:61], v[68:69], off offset:3072 nt
	global_load_dwordx4 v[62:65], v[4:5], off offset:3072 nt
	v_add_co_u32_e32 v4, vcc, 0x15c05000, v2
	v_lshl_add_u64 v[8:9], v[16:17], 0, v[8:9]
	v_lshl_add_u64 v[10:11], v[16:17], 0, v[10:11]
	v_lshl_add_u64 v[12:13], v[16:17], 0, v[12:13]
	global_load_dwordx4 v[66:69], v[6:7], off offset:3072 nt
	global_load_dwordx4 v[70:73], v[8:9], off offset:3072 nt
	global_load_dwordx4 v[74:77], v[10:11], off offset:3072 nt
	global_load_dwordx4 v[78:81], v[12:13], off offset:3072 nt
	global_load_dwordx4 v[82:85], v[88:89], off offset:3072 nt
	global_load_dwordx4 v[108:111], v[90:91], off offset:3072 nt
	global_load_dwordx4 v[112:115], v[92:93], off offset:3072 nt
	global_load_dwordx4 v[116:119], v[94:95], off offset:3072 nt
	v_addc_co_u32_e32 v5, vcc, 0, v3, vcc
	v_add_co_u32_e32 v6, vcc, 0x15c06000, v2
	global_load_dwordx4 v[120:123], v[86:87], off offset:3072 nt
	global_load_dwordx4 v[10:13], v[4:5], off offset:3072 nt
	v_addc_co_u32_e32 v7, vcc, 0, v3, vcc
	v_add_co_u32_e32 v2, vcc, 0x15c07000, v2
	v_cvt_f32_i32_e32 v96, v25
	s_nop 0
	v_addc_co_u32_e32 v3, vcc, 0, v3, vcc
	global_load_dwordx4 v[6:9], v[6:7], off offset:3072 nt
	s_nop 0
	global_load_dwordx4 v[2:5], v[2:3], off offset:3072 nt
	v_cndmask_b32_e64 v42, 1.0, 0, s[4:5]
	v_div_scale_f32 v88, s[4:5], v96, v96, 1.0
	v_div_scale_f32 v90, s[6:7], v97, v97, 1.0
	v_rcp_f32_e32 v86, v88
	v_div_scale_f32 v92, s[8:9], v98, v98, 1.0
	v_rcp_f32_e32 v87, v90
	v_div_scale_f32 v94, s[10:11], v99, v99, 1.0
	v_rcp_f32_e32 v134, v92
	v_div_scale_f32 v126, s[12:13], v100, v100, 1.0
	v_rcp_f32_e32 v135, v94
	v_div_scale_f32 v128, s[14:15], v101, v101, 1.0
	v_rcp_f32_e32 v136, v126
	v_fma_f32 v140, -v88, v86, 1.0
	v_div_scale_f32 v89, s[4:5], 1.0, v96, 1.0
	v_div_scale_f32 v130, s[16:17], v124, v124, 1.0
	v_rcp_f32_e32 v137, v128
	v_fma_f32 v141, -v90, v87, 1.0
	v_fmac_f32_e32 v86, v140, v86
	v_div_scale_f32 v91, s[6:7], 1.0, v97, 1.0
	v_div_scale_f32 v132, s[18:19], v125, v125, 1.0
	v_rcp_f32_e32 v138, v130
	v_fma_f32 v142, -v92, v134, 1.0
	v_fmac_f32_e32 v87, v141, v87
	v_mul_f32_e32 v140, v89, v86
	v_div_scale_f32 v93, s[8:9], 1.0, v98, 1.0
	v_rcp_f32_e32 v139, v132
	v_fma_f32 v143, -v94, v135, 1.0
	v_fmac_f32_e32 v134, v142, v134
	v_mul_f32_e32 v141, v91, v87
	v_fma_f32 v148, -v88, v140, v89
	v_div_scale_f32 v95, s[10:11], 1.0, v99, 1.0
	v_fma_f32 v144, -v126, v136, 1.0
	v_fmac_f32_e32 v135, v143, v135
	v_mul_f32_e32 v142, v93, v134
	v_fma_f32 v149, -v90, v141, v91
	v_fmac_f32_e32 v140, v148, v86
	v_div_scale_f32 v127, s[12:13], 1.0, v100, 1.0
	v_fma_f32 v145, -v128, v137, 1.0
	v_fmac_f32_e32 v136, v144, v136
	v_mul_f32_e32 v143, v95, v135
	v_fma_f32 v150, -v92, v142, v93
	v_fmac_f32_e32 v141, v149, v87
	v_fma_f32 v88, -v88, v140, v89
	s_mov_b64 vcc, s[4:5]
	v_div_scale_f32 v129, s[14:15], 1.0, v101, 1.0
	v_fma_f32 v146, -v130, v138, 1.0
	v_fmac_f32_e32 v137, v145, v137
	v_mul_f32_e32 v144, v127, v136
	v_fma_f32 v151, -v94, v143, v95
	v_fmac_f32_e32 v142, v150, v134
	v_fma_f32 v89, -v90, v141, v91
	v_div_fmas_f32 v86, v88, v86, v140
	s_mov_b64 vcc, s[6:7]
	v_div_scale_f32 v131, s[16:17], 1.0, v124, 1.0
	v_fma_f32 v147, -v132, v139, 1.0
	v_fmac_f32_e32 v138, v146, v138
	v_mul_f32_e32 v145, v129, v137
	v_fma_f32 v152, -v126, v144, v127
	v_fmac_f32_e32 v143, v151, v135
	v_fma_f32 v90, -v92, v142, v93
	v_div_fixup_f32 v201, v86, v96, 1.0
	v_div_fmas_f32 v86, v89, v87, v141
	s_mov_b64 vcc, s[8:9]
	v_div_scale_f32 v133, s[18:19], 1.0, v125, 1.0
	v_fmac_f32_e32 v139, v147, v139
	v_mul_f32_e32 v146, v131, v138
	v_fma_f32 v153, -v128, v145, v129
	v_fmac_f32_e32 v144, v152, v136
	v_fma_f32 v91, -v94, v143, v95
	v_div_fixup_f32 v203, v86, v97, 1.0
	v_div_fmas_f32 v86, v90, v134, v142
	s_mov_b64 vcc, s[10:11]
	v_mul_f32_e32 v147, v133, v139
	v_fma_f32 v154, -v130, v146, v131
	v_fmac_f32_e32 v145, v153, v137
	v_fma_f32 v92, -v126, v144, v127
	v_div_fixup_f32 v205, v86, v98, 1.0
	v_div_fmas_f32 v86, v91, v135, v143
	s_mov_b64 vcc, s[12:13]
	v_fma_f32 v155, -v132, v147, v133
	v_fmac_f32_e32 v146, v154, v138
	v_fma_f32 v93, -v128, v145, v129
	v_div_fixup_f32 v207, v86, v99, 1.0
	v_div_fmas_f32 v86, v92, v136, v144
	s_mov_b64 vcc, s[14:15]
	v_fmac_f32_e32 v147, v155, v139
	v_fma_f32 v94, -v130, v146, v131
	v_div_fixup_f32 v209, v86, v100, 1.0
	v_div_fmas_f32 v86, v93, v137, v145
	s_mov_b64 vcc, s[16:17]
	v_fma_f32 v95, -v132, v147, v133
	v_div_fixup_f32 v211, v86, v101, 1.0
	v_div_fmas_f32 v86, v94, v138, v146
	s_mov_b64 vcc, s[18:19]
	v_mov_b32_e32 v31, v23
	v_mov_b32_e32 v25, v23
	v_mov_b32_e32 v27, v23
	v_mov_b32_e32 v35, v23
	v_mov_b32_e32 v29, v23
	v_mov_b32_e32 v37, v23
	v_div_fixup_f32 v213, v86, v124, 1.0
	v_div_fmas_f32 v86, v95, v139, v147
	s_waitcnt vmcnt(15)
	v_and_b32_e32 v126, 0xffff0000, v50
	v_lshlrev_b32_e32 v128, 16, v51
	v_lshlrev_b32_e32 v132, 16, v52
	v_and_b32_e32 v134, 0xffff0000, v52
	v_lshlrev_b32_e32 v136, 16, v53
	v_and_b32_e32 v138, 0xffff0000, v53
	s_waitcnt vmcnt(11)
	v_and_b32_e32 v127, 0xffff0000, v66
	v_lshlrev_b32_e32 v129, 16, v67
	v_lshlrev_b32_e32 v133, 16, v68
	v_and_b32_e32 v135, 0xffff0000, v68
	v_lshlrev_b32_e32 v137, 16, v69
	v_and_b32_e32 v139, 0xffff0000, v69
	v_mov_b32_e32 v33, v23
	v_div_fixup_f32 v215, v86, v125, 1.0
	v_lshlrev_b32_e32 v124, 16, v50
	v_and_b32_e32 v130, 0xffff0000, v51
	v_lshlrev_b32_e32 v125, 16, v66
	v_and_b32_e32 v131, 0xffff0000, v67
	s_waitcnt vmcnt(10)
	v_lshlrev_b32_e32 v141, 16, v70
	v_and_b32_e32 v143, 0xffff0000, v70
	v_lshlrev_b32_e32 v145, 16, v71
	v_and_b32_e32 v147, 0xffff0000, v71
	v_lshlrev_b32_e32 v149, 16, v72
	v_and_b32_e32 v151, 0xffff0000, v72
	v_lshlrev_b32_e32 v153, 16, v73
	v_and_b32_e32 v155, 0xffff0000, v73
	s_waitcnt vmcnt(9)
	v_lshlrev_b32_e32 v157, 16, v74
	v_and_b32_e32 v159, 0xffff0000, v74
	v_lshlrev_b32_e32 v161, 16, v75
	v_and_b32_e32 v163, 0xffff0000, v75
	s_waitcnt vmcnt(6)
	v_and_b32_e32 v71, 0xffff0000, v108
	v_and_b32_e32 v73, 0xffff0000, v109
	v_and_b32_e32 v75, 0xffff0000, v110
	s_waitcnt vmcnt(5)
	v_lshlrev_b32_e32 v69, 16, v115
	s_waitcnt vmcnt(4)
	v_lshlrev_b32_e32 v53, 16, v119
	v_and_b32_e32 v51, 0xffff0000, v119
	v_pk_add_f32 v[30:31], v[30:31], v[126:127]
	v_pk_add_f32 v[24:25], v[24:25], v[128:129]
	v_pk_add_f32 v[26:27], v[26:27], v[132:133]
	v_pk_add_f32 v[34:35], v[34:35], v[134:135]
	v_pk_add_f32 v[28:29], v[28:29], v[136:137]
	v_pk_add_f32 v[36:37], v[36:37], v[138:139]
	v_mul_f32_e32 v50, v23, v127
	v_mul_f32_e32 v52, v23, v129
	v_mul_f32_e32 v68, v23, v133
	v_mul_f32_e32 v70, v23, v135
	v_mul_f32_e32 v72, v23, v137
	v_mul_f32_e32 v74, v23, v139
	v_lshlrev_b32_e32 v172, 16, v62
	v_and_b32_e32 v174, 0xffff0000, v62
	v_lshlrev_b32_e32 v176, 16, v63
	v_and_b32_e32 v178, 0xffff0000, v63
	v_lshlrev_b32_e32 v180, 16, v64
	v_and_b32_e32 v182, 0xffff0000, v64
	v_lshlrev_b32_e32 v184, 16, v65
	v_and_b32_e32 v186, 0xffff0000, v65
	v_lshlrev_b32_e32 v99, 16, v83
	v_and_b32_e32 v89, 0xffff0000, v83
	v_lshlrev_b32_e32 v95, 16, v85
	v_and_b32_e32 v93, 0xffff0000, v85
	v_lshlrev_b32_e32 v85, 16, v108
	v_lshlrev_b32_e32 v83, 16, v109
	v_and_b32_e32 v65, 0xffff0000, v115
	v_lshlrev_b32_e32 v62, 16, v113
	v_and_b32_e32 v63, 0xffff0000, v113
	v_pk_add_f32 v[108:109], v[22:23], v[124:125]
	v_pk_add_f32 v[32:33], v[32:33], v[130:131]
	v_mul_f32_e32 v22, v23, v125
	v_mul_f32_e32 v64, v23, v131
	s_waitcnt vmcnt(3)
	v_lshlrev_b32_e32 v98, 16, v121
	v_and_b32_e32 v88, 0xffff0000, v121
	v_lshlrev_b32_e32 v94, 16, v123
	v_and_b32_e32 v92, 0xffff0000, v123
	v_fma_f32 v113, v201, v30, -v126
	v_fma_f32 v115, v201, v24, -v128
	v_fma_f32 v119, v201, v26, -v132
	v_fma_f32 v121, v201, v34, -v134
	v_fma_f32 v123, v201, v28, -v136
	v_fma_f32 v125, v201, v36, -v138
	v_pk_add_f32 v[30:31], v[30:31], v[50:51] op_sel_hi:[1,0] neg_lo:[0,1] neg_hi:[0,1]
	v_pk_add_f32 v[24:25], v[24:25], v[52:53] op_sel_hi:[1,0] neg_lo:[0,1] neg_hi:[0,1]
	v_pk_add_f32 v[26:27], v[26:27], v[68:69] op_sel_hi:[1,0] neg_lo:[0,1] neg_hi:[0,1]
	v_pk_add_f32 v[34:35], v[34:35], v[70:71] op_sel_hi:[1,0] neg_lo:[0,1] neg_hi:[0,1]
	v_pk_add_f32 v[28:29], v[28:29], v[72:73] op_sel_hi:[1,0] neg_lo:[0,1] neg_hi:[0,1]
	v_pk_add_f32 v[36:37], v[36:37], v[74:75] op_sel_hi:[1,0] neg_lo:[0,1] neg_hi:[0,1]
	v_and_b32_e32 v142, 0xffff0000, v54
	v_lshlrev_b32_e32 v144, 16, v55
	v_lshlrev_b32_e32 v148, 16, v56
	v_and_b32_e32 v150, 0xffff0000, v56
	v_lshlrev_b32_e32 v152, 16, v57
	v_and_b32_e32 v154, 0xffff0000, v57
	v_lshlrev_b32_e32 v156, 16, v58
	v_and_b32_e32 v158, 0xffff0000, v58
	v_lshlrev_b32_e32 v160, 16, v59
	v_and_b32_e32 v162, 0xffff0000, v59
	v_lshlrev_b32_e32 v165, 16, v76
	v_and_b32_e32 v167, 0xffff0000, v76
	v_lshlrev_b32_e32 v169, 16, v77
	v_and_b32_e32 v171, 0xffff0000, v77
	v_lshlrev_b32_e32 v173, 16, v78
	v_and_b32_e32 v175, 0xffff0000, v78
	v_lshlrev_b32_e32 v177, 16, v79
	v_and_b32_e32 v179, 0xffff0000, v79
	v_lshlrev_b32_e32 v181, 16, v80
	v_and_b32_e32 v183, 0xffff0000, v80
	v_lshlrev_b32_e32 v101, 16, v82
	v_and_b32_e32 v87, 0xffff0000, v82
	v_lshlrev_b32_e32 v97, 16, v84
	v_and_b32_e32 v91, 0xffff0000, v84
	v_lshlrev_b32_e32 v79, 16, v111
	v_and_b32_e32 v77, 0xffff0000, v111
	v_lshlrev_b32_e32 v58, 16, v117
	v_and_b32_e32 v59, 0xffff0000, v117
	v_fma_f32 v111, v201, v108, -v124
	v_fma_f32 v117, v201, v32, -v130
	v_pk_add_f32 v[22:23], v[108:109], v[22:23] op_sel_hi:[1,0] neg_lo:[0,1] neg_hi:[0,1]
	v_pk_add_f32 v[32:33], v[32:33], v[64:65] op_sel_hi:[1,0] neg_lo:[0,1] neg_hi:[0,1]
	s_waitcnt vmcnt(2)
	v_lshlrev_b32_e32 v84, 16, v10
	v_and_b32_e32 v70, 0xffff0000, v10
	v_lshlrev_b32_e32 v82, 16, v11
	v_and_b32_e32 v72, 0xffff0000, v11
	v_lshlrev_b32_e32 v80, 16, v12
	v_and_b32_e32 v74, 0xffff0000, v12
	v_lshlrev_b32_e32 v78, 16, v13
	v_and_b32_e32 v76, 0xffff0000, v13
	v_cvt_pk_bf16_f32 v10, v111, v113
	v_cvt_pk_bf16_f32 v11, v115, v117
	v_cvt_pk_bf16_f32 v12, v119, v121
	v_cvt_pk_bf16_f32 v13, v123, v125
	v_mov_b32_e32 v31, v195
	v_mov_b32_e32 v25, v195
	v_mov_b32_e32 v27, v195
	v_mov_b32_e32 v35, v195
	v_mov_b32_e32 v29, v195
	v_mov_b32_e32 v37, v195
	v_lshlrev_b32_e32 v140, 16, v54
	v_and_b32_e32 v146, 0xffff0000, v55
	v_mov_b32_e32 v23, v195
	v_mov_b32_e32 v33, v195
	global_store_dwordx4 v[48:49], v[10:13], off offset:1024
	v_pk_add_f32 v[28:29], v[28:29], v[152:153]
	v_lshlrev_b32_e32 v164, 16, v60
	v_pk_add_f32 v[10:11], v[30:31], v[142:143]
	v_pk_add_f32 v[12:13], v[24:25], v[144:145]
	v_pk_add_f32 v[24:25], v[26:27], v[148:149]
	v_pk_add_f32 v[26:27], v[34:35], v[150:151]
	v_pk_add_f32 v[30:31], v[36:37], v[154:155]
	v_and_b32_e32 v166, 0xffff0000, v60
	v_lshlrev_b32_e32 v168, 16, v61
	v_and_b32_e32 v170, 0xffff0000, v61
	v_lshlrev_b32_e32 v185, 16, v81
	v_and_b32_e32 v187, 0xffff0000, v81
	v_lshlrev_b32_e32 v81, 16, v110
	v_lshlrev_b32_e32 v60, 16, v112
	v_and_b32_e32 v61, 0xffff0000, v112
	v_lshlrev_b32_e32 v54, 16, v116
	v_and_b32_e32 v55, 0xffff0000, v116
	v_lshlrev_b32_e32 v66, 16, v114
	v_and_b32_e32 v67, 0xffff0000, v114
	v_lshlrev_b32_e32 v56, 16, v118
	v_and_b32_e32 v57, 0xffff0000, v118
	v_mul_f32_e32 v110, v195, v141
	v_mul_f32_e32 v112, v195, v143
	v_mul_f32_e32 v114, v195, v145
	v_mul_f32_e32 v116, v195, v147
	v_mul_f32_e32 v118, v195, v149
	v_mul_f32_e32 v196, v195, v151
	v_mul_f32_e32 v198, v195, v153
	v_mul_f32_e32 v200, v195, v155
	s_waitcnt vmcnt(2)
	v_lshlrev_b32_e32 v68, 16, v9
	v_and_b32_e32 v64, 0xffff0000, v9
	v_lshlrev_b32_e32 v238, 16, v8
	v_and_b32_e32 v239, 0xffff0000, v8
	v_pk_add_f32 v[8:9], v[22:23], v[140:141]
	v_pk_add_f32 v[22:23], v[32:33], v[146:147]
	v_fma_f32 v111, v203, v26, -v150
	v_fma_f32 v113, v203, v28, -v152
	v_fma_f32 v115, v203, v30, -v154
	s_waitcnt vmcnt(1)
	v_lshlrev_b32_e32 v32, 16, v2
	v_and_b32_e32 v33, 0xffff0000, v2
	v_lshlrev_b32_e32 v34, 16, v3
	v_and_b32_e32 v35, 0xffff0000, v3
	v_lshlrev_b32_e32 v36, 16, v4
	v_and_b32_e32 v37, 0xffff0000, v4
	v_lshlrev_b32_e32 v52, 16, v5
	v_and_b32_e32 v50, 0xffff0000, v5
	v_fma_f32 v2, v203, v8, -v140
	v_fma_f32 v3, v203, v10, -v142
	v_fma_f32 v4, v203, v12, -v144
	v_fma_f32 v5, v203, v22, -v146
	v_fma_f32 v109, v203, v24, -v148
	v_pk_add_f32 v[8:9], v[8:9], v[110:111] op_sel_hi:[1,0] neg_lo:[0,1] neg_hi:[0,1]
	v_pk_add_f32 v[10:11], v[10:11], v[112:113] op_sel_hi:[1,0] neg_lo:[0,1] neg_hi:[0,1]
	v_pk_add_f32 v[12:13], v[12:13], v[114:115] op_sel_hi:[1,0] neg_lo:[0,1] neg_hi:[0,1]
	v_pk_add_f32 v[22:23], v[22:23], v[116:117] op_sel_hi:[1,0] neg_lo:[0,1] neg_hi:[0,1]
	v_pk_add_f32 v[24:25], v[24:25], v[118:119] op_sel_hi:[1,0] neg_lo:[0,1] neg_hi:[0,1]
	v_pk_add_f32 v[26:27], v[26:27], v[196:197] op_sel_hi:[1,0] neg_lo:[0,1] neg_hi:[0,1]
	v_pk_add_f32 v[28:29], v[28:29], v[198:199] op_sel_hi:[1,0] neg_lo:[0,1] neg_hi:[0,1]
	v_pk_add_f32 v[30:31], v[30:31], v[200:201] op_sel_hi:[1,0] neg_lo:[0,1] neg_hi:[0,1]
	v_cvt_pk_bf16_f32 v2, v2, v3
	v_cvt_pk_bf16_f32 v3, v4, v5
	v_cvt_pk_bf16_f32 v4, v109, v111
	v_cvt_pk_bf16_f32 v5, v113, v115
	v_mov_b32_e32 v9, v197
	v_mov_b32_e32 v11, v197
	v_mov_b32_e32 v13, v197
	v_mov_b32_e32 v23, v197
	v_mov_b32_e32 v25, v197
	v_mov_b32_e32 v27, v197
	v_mov_b32_e32 v29, v197
	v_mov_b32_e32 v31, v197
	v_mul_f32_e32 v202, v197, v157
	v_mul_f32_e32 v204, v197, v159
	v_mul_f32_e32 v206, v197, v161
	v_mul_f32_e32 v208, v197, v163
	v_mul_f32_e32 v210, v197, v165
	v_mul_f32_e32 v212, v197, v167
	v_mul_f32_e32 v214, v197, v169
	v_mul_f32_e32 v216, v197, v171
	global_store_dwordx4 v[48:49], v[2:5], off offset:3072
	v_lshlrev_b32_e32 v100, 16, v120
	v_mul_f32_e32 v218, v199, v173
	v_pk_add_f32 v[2:3], v[8:9], v[156:157]
	v_pk_add_f32 v[4:5], v[10:11], v[158:159]
	v_pk_add_f32 v[8:9], v[12:13], v[160:161]
	v_pk_add_f32 v[10:11], v[22:23], v[162:163]
	v_pk_add_f32 v[12:13], v[24:25], v[164:165]
	v_pk_add_f32 v[22:23], v[26:27], v[166:167]
	v_pk_add_f32 v[24:25], v[28:29], v[168:169]
	v_pk_add_f32 v[26:27], v[30:31], v[170:171]
	v_fma_f32 v109, v205, v8, -v160
	v_fma_f32 v110, v205, v10, -v162
	v_fma_f32 v111, v205, v12, -v164
	v_fma_f32 v112, v205, v22, -v166
	v_fma_f32 v113, v205, v24, -v168
	v_fma_f32 v114, v205, v26, -v170
	v_pk_add_f32 v[28:29], v[2:3], v[202:203] op_sel_hi:[1,0] neg_lo:[0,1] neg_hi:[0,1]
	v_pk_add_f32 v[30:31], v[4:5], v[204:205] op_sel_hi:[1,0] neg_lo:[0,1] neg_hi:[0,1]
	v_pk_add_f32 v[8:9], v[8:9], v[206:207] op_sel_hi:[1,0] neg_lo:[0,1] neg_hi:[0,1]
	v_pk_add_f32 v[10:11], v[10:11], v[208:209] op_sel_hi:[1,0] neg_lo:[0,1] neg_hi:[0,1]
	v_pk_add_f32 v[12:13], v[12:13], v[210:211] op_sel_hi:[1,0] neg_lo:[0,1] neg_hi:[0,1]
	v_pk_add_f32 v[22:23], v[22:23], v[212:213] op_sel_hi:[1,0] neg_lo:[0,1] neg_hi:[0,1]
	v_pk_add_f32 v[24:25], v[24:25], v[214:215] op_sel_hi:[1,0] neg_lo:[0,1] neg_hi:[0,1]
	v_pk_add_f32 v[26:27], v[26:27], v[216:217] op_sel_hi:[1,0] neg_lo:[0,1] neg_hi:[0,1]
	v_fma_f32 v48, v205, v2, -v156
	v_fma_f32 v49, v205, v4, -v158
	v_cvt_pk_bf16_f32 v2, v48, v49
	v_cvt_pk_bf16_f32 v3, v109, v110
	v_cvt_pk_bf16_f32 v4, v111, v112
	v_cvt_pk_bf16_f32 v5, v113, v114
	v_mov_b32_e32 v29, v199
	v_mov_b32_e32 v31, v199
	v_mov_b32_e32 v9, v199
	v_mov_b32_e32 v11, v199
	v_mov_b32_e32 v13, v199
	v_mov_b32_e32 v23, v199
	v_mov_b32_e32 v25, v199
	v_mov_b32_e32 v27, v199
	v_and_b32_e32 v86, 0xffff0000, v120
	v_mul_f32_e32 v120, v199, v175
	v_mul_f32_e32 v220, v199, v177
	v_mul_f32_e32 v222, v199, v179
	v_lshlrev_b32_e32 v96, 16, v122
	v_mul_f32_e32 v224, v199, v181
	v_and_b32_e32 v90, 0xffff0000, v122
	v_mul_f32_e32 v122, v199, v183
	v_mul_f32_e32 v226, v199, v185
	v_mul_f32_e32 v228, v199, v187
	global_store_dwordx4 v[46:47], v[2:5], off offset:1024
	v_pk_add_f32 v[8:9], v[8:9], v[176:177]
	v_pk_add_f32 v[10:11], v[10:11], v[178:179]
	v_pk_add_f32 v[2:3], v[28:29], v[172:173]
	v_pk_add_f32 v[4:5], v[30:31], v[174:175]
	v_pk_add_f32 v[12:13], v[12:13], v[180:181]
	v_pk_add_f32 v[22:23], v[22:23], v[182:183]
	v_pk_add_f32 v[24:25], v[24:25], v[184:185]
	v_pk_add_f32 v[26:27], v[26:27], v[186:187]
	v_fma_f32 v109, v207, v8, -v176
	v_fma_f32 v110, v207, v10, -v178
	v_fma_f32 v111, v207, v12, -v180
	v_fma_f32 v112, v207, v22, -v182
	v_fma_f32 v113, v207, v24, -v184
	v_fma_f32 v114, v207, v26, -v186
	v_pk_add_f32 v[28:29], v[2:3], v[218:219] op_sel_hi:[1,0] neg_lo:[0,1] neg_hi:[0,1]
	v_pk_add_f32 v[30:31], v[4:5], v[120:121] op_sel_hi:[1,0] neg_lo:[0,1] neg_hi:[0,1]
	v_pk_add_f32 v[8:9], v[8:9], v[220:221] op_sel_hi:[1,0] neg_lo:[0,1] neg_hi:[0,1]
	v_pk_add_f32 v[10:11], v[10:11], v[222:223] op_sel_hi:[1,0] neg_lo:[0,1] neg_hi:[0,1]
	v_pk_add_f32 v[12:13], v[12:13], v[224:225] op_sel_hi:[1,0] neg_lo:[0,1] neg_hi:[0,1]
	v_pk_add_f32 v[22:23], v[22:23], v[122:123] op_sel_hi:[1,0] neg_lo:[0,1] neg_hi:[0,1]
	v_pk_add_f32 v[24:25], v[24:25], v[226:227] op_sel_hi:[1,0] neg_lo:[0,1] neg_hi:[0,1]
	v_pk_add_f32 v[26:27], v[26:27], v[228:229] op_sel_hi:[1,0] neg_lo:[0,1] neg_hi:[0,1]
	v_fma_f32 v48, v207, v2, -v172
	v_fma_f32 v49, v207, v4, -v174
	v_cvt_pk_bf16_f32 v2, v48, v49
	v_cvt_pk_bf16_f32 v3, v109, v110
	v_cvt_pk_bf16_f32 v4, v111, v112
	v_cvt_pk_bf16_f32 v5, v113, v114
	v_mov_b32_e32 v29, v107
	v_mov_b32_e32 v31, v107
	v_mov_b32_e32 v9, v107
	v_mov_b32_e32 v11, v107
	v_mov_b32_e32 v13, v107
	v_mov_b32_e32 v23, v107
	v_mov_b32_e32 v25, v107
	v_mov_b32_e32 v27, v107
	v_mul_f32_e32 v230, v107, v101
	v_mul_f32_e32 v232, v107, v87
	v_mul_f32_e32 v234, v107, v99
	v_mul_f32_e32 v124, v107, v89
	v_mul_f32_e32 v126, v107, v97
	v_mul_f32_e32 v128, v107, v91
	v_mul_f32_e32 v130, v107, v95
	v_mul_f32_e32 v132, v107, v93
	global_store_dwordx4 v[46:47], v[2:5], off offset:3072
	v_pk_add_f32 v[8:9], v[8:9], v[98:99]
	v_pk_add_f32 v[10:11], v[10:11], v[88:89]
	v_pk_add_f32 v[2:3], v[28:29], v[100:101]
	v_pk_add_f32 v[4:5], v[30:31], v[86:87]
	v_pk_add_f32 v[12:13], v[12:13], v[96:97]
	v_pk_add_f32 v[22:23], v[22:23], v[90:91]
	v_pk_add_f32 v[24:25], v[24:25], v[94:95]
	v_pk_add_f32 v[26:27], v[26:27], v[92:93]
	v_fma_f32 v47, v209, v4, -v86
	v_fma_f32 v48, v209, v8, -v98
	v_fma_f32 v49, v209, v10, -v88
	v_fma_f32 v86, v209, v12, -v96
	v_fma_f32 v87, v209, v22, -v90
	v_fma_f32 v88, v209, v24, -v94
	v_fma_f32 v89, v209, v26, -v92
	v_pk_add_f32 v[28:29], v[2:3], v[230:231] op_sel_hi:[1,0] neg_lo:[0,1] neg_hi:[0,1]
	v_pk_add_f32 v[30:31], v[4:5], v[232:233] op_sel_hi:[1,0] neg_lo:[0,1] neg_hi:[0,1]
	v_pk_add_f32 v[8:9], v[8:9], v[234:235] op_sel_hi:[1,0] neg_lo:[0,1] neg_hi:[0,1]
	v_pk_add_f32 v[10:11], v[10:11], v[124:125] op_sel_hi:[1,0] neg_lo:[0,1] neg_hi:[0,1]
	v_pk_add_f32 v[12:13], v[12:13], v[126:127] op_sel_hi:[1,0] neg_lo:[0,1] neg_hi:[0,1]
	v_pk_add_f32 v[22:23], v[22:23], v[128:129] op_sel_hi:[1,0] neg_lo:[0,1] neg_hi:[0,1]
	v_pk_add_f32 v[24:25], v[24:25], v[130:131] op_sel_hi:[1,0] neg_lo:[0,1] neg_hi:[0,1]
	v_pk_add_f32 v[26:27], v[26:27], v[132:133] op_sel_hi:[1,0] neg_lo:[0,1] neg_hi:[0,1]
	v_fma_f32 v46, v209, v2, -v100
	v_cvt_pk_bf16_f32 v2, v46, v47
	v_cvt_pk_bf16_f32 v3, v48, v49
	v_cvt_pk_bf16_f32 v4, v86, v87
	v_cvt_pk_bf16_f32 v5, v88, v89
	v_mov_b32_e32 v29, v106
	v_mov_b32_e32 v31, v106
	v_mov_b32_e32 v9, v106
	v_mov_b32_e32 v11, v106
	v_mov_b32_e32 v13, v106
	v_mov_b32_e32 v23, v106
	v_mov_b32_e32 v25, v106
	v_mov_b32_e32 v27, v106
	v_mul_f32_e32 v108, v106, v79
	v_mul_f32_e32 v134, v106, v77
	global_store_dwordx4 v[40:41], v[2:5], off offset:1024
	v_pk_add_f32 v[46:47], v[28:29], v[84:85]
	v_pk_add_f32 v[48:49], v[10:11], v[72:73]
	v_pk_mul_f32 v[2:3], v[28:29], v[84:85]
	v_pk_add_f32 v[4:5], v[30:31], v[70:71]
	v_pk_mul_f32 v[28:29], v[30:31], v[70:71]
	v_pk_add_f32 v[30:31], v[8:9], v[82:83]
	v_pk_mul_f32 v[8:9], v[8:9], v[82:83]
	v_pk_mul_f32 v[10:11], v[10:11], v[72:73]
	v_pk_add_f32 v[86:87], v[12:13], v[80:81]
	v_pk_mul_f32 v[12:13], v[12:13], v[80:81]
	v_pk_add_f32 v[88:89], v[22:23], v[74:75]
	v_pk_mul_f32 v[22:23], v[22:23], v[74:75]
	v_pk_add_f32 v[24:25], v[24:25], v[78:79]
	v_pk_add_f32 v[26:27], v[26:27], v[76:77]
	v_fma_f32 v2, v211, v46, -v84
	v_fma_f32 v5, v211, v4, -v70
	v_fma_f32 v8, v211, v30, -v82
	v_fma_f32 v12, v211, v48, -v72
	v_fma_f32 v71, v211, v24, -v78
	v_fma_f32 v72, v211, v26, -v76
	v_pk_add_f32 v[24:25], v[24:25], v[108:109] op_sel_hi:[1,0] neg_lo:[0,1] neg_hi:[0,1]
	v_pk_add_f32 v[26:27], v[26:27], v[134:135] op_sel_hi:[1,0] neg_lo:[0,1] neg_hi:[0,1]
	v_mov_b32_e32 v47, v4
	v_mov_b32_e32 v28, v3
	v_mov_b32_e32 v31, v48
	v_mov_b32_e32 v10, v9
	v_mov_b32_e32 v87, v88
	v_mov_b32_e32 v22, v13
	v_lshlrev_b32_e32 v236, 16, v6
	v_and_b32_e32 v237, 0xffff0000, v6
	v_lshlrev_b32_e32 v6, 16, v7
	v_and_b32_e32 v7, 0xffff0000, v7
	v_fma_f32 v49, v211, v86, -v80
	v_fma_f32 v70, v211, v88, -v74
	v_cvt_pk_bf16_f32 v2, v2, v5
	v_cvt_pk_bf16_f32 v3, v8, v12
	v_cvt_pk_bf16_f32 v4, v49, v70
	v_cvt_pk_bf16_f32 v5, v71, v72
	v_mov_b32_e32 v25, v44
	v_mov_b32_e32 v27, v44
	v_pk_add_f32 v[8:9], v[46:47], v[28:29] neg_lo:[0,1] neg_hi:[0,1]
	v_pk_add_f32 v[10:11], v[30:31], v[10:11] neg_lo:[0,1] neg_hi:[0,1]
	v_pk_add_f32 v[12:13], v[86:87], v[22:23] neg_lo:[0,1] neg_hi:[0,1]
	v_mul_f32_e32 v136, v44, v69
	v_mul_f32_e32 v138, v44, v65
	global_store_dwordx4 v[40:41], v[2:5], off offset:3072
	v_pk_add_f32 v[8:9], v[8:9], v[236:237]
	v_pk_add_f32 v[10:11], v[10:11], v[6:7]
	v_pk_add_f32 v[2:3], v[24:25], v[68:69]
	v_pk_add_f32 v[4:5], v[26:27], v[64:65]
	v_pk_add_f32 v[12:13], v[12:13], v[238:239]
	v_fma_f32 v24, v213, v8, -v236
	v_fma_f32 v25, v213, v9, -v237
	v_pk_fma_f32 v[8:9], v[44:45], v[60:61], v[8:9] op_sel_hi:[0,1,1] neg_lo:[1,0,0] neg_hi:[1,0,0]
	v_fma_f32 v26, v213, v10, -v6
	v_fma_f32 v27, v213, v11, -v7
	v_pk_fma_f32 v[6:7], v[44:45], v[62:63], v[10:11] op_sel_hi:[0,1,1] neg_lo:[1,0,0] neg_hi:[1,0,0]
	v_fma_f32 v30, v213, v12, -v238
	v_fma_f32 v31, v213, v13, -v239
	v_pk_fma_f32 v[10:11], v[44:45], v[66:67], v[12:13] op_sel_hi:[0,1,1] neg_lo:[1,0,0] neg_hi:[1,0,0]
	v_pk_add_f32 v[12:13], v[2:3], v[136:137] op_sel_hi:[1,0] neg_lo:[0,1] neg_hi:[0,1]
	v_pk_add_f32 v[28:29], v[4:5], v[138:139] op_sel_hi:[1,0] neg_lo:[0,1] neg_hi:[0,1]
	v_fma_f32 v22, v213, v2, -v68
	v_fma_f32 v23, v213, v4, -v64
	v_cvt_pk_bf16_f32 v2, v24, v25
	v_pk_add_f32 v[8:9], v[8:9], v[32:33]
	v_pk_add_f32 v[6:7], v[6:7], v[34:35]
	v_cvt_pk_bf16_f32 v3, v26, v27
	v_pk_add_f32 v[10:11], v[10:11], v[36:37]
	v_cvt_pk_bf16_f32 v4, v30, v31
	v_cvt_pk_bf16_f32 v5, v22, v23
	v_mov_b32_e32 v13, v42
	v_mov_b32_e32 v29, v42
	v_fma_f32 v30, v215, v8, -v32
	v_fma_f32 v31, v215, v9, -v33
	v_pk_fma_f32 v[22:23], v[42:43], v[54:55], v[8:9] op_sel_hi:[0,1,1] neg_lo:[1,0,0] neg_hi:[1,0,0]
	v_fma_f32 v32, v215, v6, -v34
	v_fma_f32 v33, v215, v7, -v35
	v_pk_fma_f32 v[24:25], v[42:43], v[58:59], v[6:7] op_sel_hi:[0,1,1] neg_lo:[1,0,0] neg_hi:[1,0,0]
	v_fma_f32 v34, v215, v10, -v36
	v_fma_f32 v35, v215, v11, -v37
	global_store_dwordx4 v[38:39], v[2:5], off offset:1024
	v_pk_fma_f32 v[26:27], v[42:43], v[56:57], v[10:11] op_sel_hi:[0,1,1] neg_lo:[1,0,0] neg_hi:[1,0,0]
	v_pk_add_f32 v[6:7], v[12:13], v[52:53]
	v_pk_mul_f32 v[4:5], v[12:13], v[52:53]
	v_pk_add_f32 v[8:9], v[28:29], v[50:51]
	v_pk_mul_f32 v[10:11], v[28:29], v[50:51]
	v_mov_b32_e32 v7, v8
	v_mov_b32_e32 v10, v5
	s_add_i32 s38, s37, 8
	v_pk_add_f32 v[28:29], v[6:7], v[10:11] neg_lo:[0,1] neg_hi:[0,1]
	v_lshl_add_u64 v[18:19], v[18:19], 0, s[30:31]
	v_lshl_add_u64 v[20:21], v[20:21], 0, s[34:35]
	s_cmp_gt_u32 s37, 23
	s_mov_b32 s37, s38
	v_cvt_pk_bf16_f32 v2, v30, v31
	v_cvt_pk_bf16_f32 v3, v32, v33
	v_cvt_pk_bf16_f32 v4, v34, v35
	v_mov_b32_e32 v30, v23
	v_mov_b32_e32 v32, v25
	v_mov_b32_e32 v34, v27
	v_mov_b32_e32 v36, v29
	v_fma_f32 v9, v215, v6, -v52
	v_fma_f32 v12, v215, v8, -v50
	v_cvt_pk_bf16_f32 v5, v9, v12
	global_store_dwordx4 v[38:39], v[2:5], off offset:3072
	s_cbranch_scc0 .LBB0_299
	v_add_u32_e32 v43, s86, v43
	v_cmp_lt_i32_e32 vcc, s36, v43
	s_or_b64 s[26:27], vcc, s[26:27]
	v_add_u32_e32 v45, s0, v45
	s_andn2_b64 exec, exec, s[26:27]
	s_cbranch_execnz .LBB0_294
